# layer1_rp1_combine_handwritten_pipelined
# speedup vs baseline: 1.0215x; 1.0135x over previous
.LBB0_122:
	v_readlane_b32 s8, v253, 40
	v_writelane_b32 v254, s6, 20
	s_xor_b64 s[24:25], s[6:7], -1
	v_readlane_b32 s22, v253, 54
	v_readlane_b32 s23, v253, 55
	s_add_u32 s0, s22, s4
	s_addc_u32 s1, s23, s5
	v_writelane_b32 v254, s7, 21
	s_add_u32 s6, s0, 0x23000000
	v_and_b32_e32 v134, 63, v2
	s_addc_u32 s7, s1, 0
	s_lshl_b32 s26, s28, 3
	v_readlane_b32 s2, v253, 29
	v_writelane_b32 v254, s24, 18
	s_add_i32 s8, s26, s2
	s_lshl_b32 s29, s27, 3
	s_mov_b64 s[2:3], -1
	v_writelane_b32 v254, s25, 19
	s_and_b64 vcc, exec, s[24:25]
	v_lshlrev_b32_e32 v132, 2, v134
	v_readlane_b32 s9, v253, 41
	v_readlane_b32 s10, v253, 42
	v_readlane_b32 s11, v253, 43
	v_readlane_b32 s12, v253, 44
	v_readlane_b32 s13, v253, 45
	v_readlane_b32 s14, v253, 46
	v_readlane_b32 s15, v253, 47
	v_readlane_b32 s16, v253, 48
	v_readlane_b32 s17, v253, 49
	v_readlane_b32 s18, v253, 50
	v_readlane_b32 s19, v253, 51
	v_readlane_b32 s20, v253, 52
	v_readlane_b32 s21, v253, 53
	s_cbranch_vccz .LBB0_164
	v_lshlrev_b32_e32 v22, 3, v134
	s_mov_b32 s2, s8
	s_lshl_b32 s16, s29, 1
	s_add_u32 s10, s0, 0x400000
	s_addc_u32 s11, s1, 0
	s_add_u32 s12, s0, 0x4a000000
	s_addc_u32 s13, s1, 0
	s_add_u32 s14, s0, 0x27000000
	s_addc_u32 s15, s1, 0
	s_cmp_lt_i32 s2, 0x8000
	s_cbranch_scc0 .LBB0_163
	s_lshl_b32 s22, s2, 11
	s_add_u32 s22, s12, s22
	s_addc_u32 s23, s13, 0
	s_lshl_b32 s24, s2, 6
	s_add_u32 s24, s10, s24
	s_addc_u32 s25, s11, 0
	global_load_dwordx2 v[2:3], v22, s[22:23]
	global_load_dwordx2 v[4:5], v22, s[22:23] offset:512
	global_load_dwordx2 v[6:7], v22, s[22:23] offset:1024
	global_load_dwordx2 v[8:9], v22, s[22:23] offset:1536
	global_load_dword v18, v132, s[24:25]
	s_add_i32 s31, s2, s29
	s_cmp_lt_i32 s31, 0x8000
	s_cbranch_scc0 .Lrp1_pf_first
	s_lshl_b32 s22, s31, 11
	s_add_u32 s22, s12, s22
	s_addc_u32 s23, s13, 0
	s_lshl_b32 s24, s31, 6
	s_add_u32 s24, s10, s24
	s_addc_u32 s25, s11, 0
	global_load_dwordx2 v[10:11], v22, s[22:23]
	global_load_dwordx2 v[12:13], v22, s[22:23] offset:512
	global_load_dwordx2 v[14:15], v22, s[22:23] offset:1024
	global_load_dwordx2 v[16:17], v22, s[22:23] offset:1536
	global_load_dword v19, v132, s[24:25]
.Lrp1_pf_first:
	s_mov_b32 s18, 0
.Lrp1_loop:
	s_add_i32 s3, s2, s29
	s_cmp_lt_i32 s3, 0x8000
	s_cselect_b32 s17, 1, 0
	s_cmp_lg_u32 s18, 0
	s_cbranch_scc1 .Lrp1_nowait
	s_waitcnt vmcnt(0)
.Lrp1_nowait:
	v_lshlrev_b32_e32 v24, 16, v2
	v_and_b32_e32 v25, 0xffff0000, v2
	v_lshlrev_b32_e32 v26, 16, v3
	v_and_b32_e32 v27, 0xffff0000, v3
	v_lshlrev_b32_e32 v28, 16, v4
	v_and_b32_e32 v29, 0xffff0000, v4
	v_lshlrev_b32_e32 v30, 16, v5
	v_and_b32_e32 v31, 0xffff0000, v5
	v_lshlrev_b32_e32 v32, 16, v6
	v_and_b32_e32 v33, 0xffff0000, v6
	v_lshlrev_b32_e32 v34, 16, v7
	v_and_b32_e32 v35, 0xffff0000, v7
	v_lshlrev_b32_e32 v36, 16, v8
	v_and_b32_e32 v37, 0xffff0000, v8
	v_lshlrev_b32_e32 v38, 16, v9
	v_and_b32_e32 v39, 0xffff0000, v9
	v_lshlrev_b32_e32 v40, 16, v10
	v_and_b32_e32 v41, 0xffff0000, v10
	v_lshlrev_b32_e32 v42, 16, v11
	v_and_b32_e32 v43, 0xffff0000, v11
	v_lshlrev_b32_e32 v44, 16, v12
	v_and_b32_e32 v45, 0xffff0000, v12
	v_lshlrev_b32_e32 v46, 16, v13
	v_and_b32_e32 v47, 0xffff0000, v13
	v_lshlrev_b32_e32 v48, 16, v14
	v_and_b32_e32 v49, 0xffff0000, v14
	v_lshlrev_b32_e32 v50, 16, v15
	v_and_b32_e32 v51, 0xffff0000, v15
	v_lshlrev_b32_e32 v52, 16, v16
	v_and_b32_e32 v53, 0xffff0000, v16
	v_lshlrev_b32_e32 v54, 16, v17
	v_and_b32_e32 v55, 0xffff0000, v17
	v_mov_b32_e32 v20, v18
	v_mov_b32_e32 v21, v19
	v_cmp_lt_i32_e32 vcc, -1, v20
	s_and_b32 s19, vcc_lo, 0xffff
	v_cmp_lt_i32_e32 vcc, -1, v21
	s_and_b32 s20, vcc_lo, 0xffff
	s_cmp_eq_u32 s17, 0
	s_cselect_b32 s20, 0, s20
	s_add_i32 s30, s2, s16
	s_cmp_lt_i32 s30, 0x8000
	s_cbranch_scc0 .Lrp1_pf_next
	s_lshl_b32 s22, s30, 11
	s_add_u32 s22, s12, s22
	s_addc_u32 s23, s13, 0
	s_lshl_b32 s24, s30, 6
	s_add_u32 s24, s10, s24
	s_addc_u32 s25, s11, 0
	global_load_dwordx2 v[2:3], v22, s[22:23]
	global_load_dwordx2 v[4:5], v22, s[22:23] offset:512
	global_load_dwordx2 v[6:7], v22, s[22:23] offset:1024
	global_load_dwordx2 v[8:9], v22, s[22:23] offset:1536
	global_load_dword v18, v132, s[24:25]
	s_add_i32 s31, s30, s29
	s_cmp_lt_i32 s31, 0x8000
	s_cbranch_scc0 .Lrp1_pf_next
	s_lshl_b32 s22, s31, 11
	s_add_u32 s22, s12, s22
	s_addc_u32 s23, s13, 0
	s_lshl_b32 s24, s31, 6
	s_add_u32 s24, s10, s24
	s_addc_u32 s25, s11, 0
	global_load_dwordx2 v[10:11], v22, s[22:23]
	global_load_dwordx2 v[12:13], v22, s[22:23] offset:512
	global_load_dwordx2 v[14:15], v22, s[22:23] offset:1024
	global_load_dwordx2 v[16:17], v22, s[22:23] offset:1536
	global_load_dword v19, v132, s[24:25]
.Lrp1_pf_next:
	s_mov_b32 s18, 0
	s_or_b32 s0, s19, s20
	s_cmp_eq_u32 s0, 0
	s_cbranch_scc1 .Lrp1_rounds_done
.Lrp1_round:
	s_add_i32 s18, s18, 1
	s_mov_b32 s21, 0
	s_cmp_eq_u32 s19, 0
	s_cbranch_scc1 .Lrp1_iss_A_done
	s_ff1_i32_b32 s0, s19
	s_bitset0_b32 s19, s0
	v_readlane_b32 s1, v20, s0
	s_lshl_b32 s1, s1, 11
	s_add_u32 s22, s14, s1
	s_addc_u32 s23, s15, 0
	global_load_dwordx2 v[56:57], v22, s[22:23]
	global_load_dwordx2 v[58:59], v22, s[22:23] offset:512
	global_load_dwordx2 v[60:61], v22, s[22:23] offset:1024
	global_load_dwordx2 v[62:63], v22, s[22:23] offset:1536
	s_bitset1_b32 s21, 0
	s_cmp_eq_u32 s19, 0
	s_cbranch_scc1 .Lrp1_iss_A_done
	s_ff1_i32_b32 s0, s19
	s_bitset0_b32 s19, s0
	v_readlane_b32 s1, v20, s0
	s_lshl_b32 s1, s1, 11
	s_add_u32 s22, s14, s1
	s_addc_u32 s23, s15, 0
	global_load_dwordx2 v[64:65], v22, s[22:23]
	global_load_dwordx2 v[66:67], v22, s[22:23] offset:512
	global_load_dwordx2 v[68:69], v22, s[22:23] offset:1024
	global_load_dwordx2 v[70:71], v22, s[22:23] offset:1536
	s_bitset1_b32 s21, 1
	s_cmp_eq_u32 s19, 0
	s_cbranch_scc1 .Lrp1_iss_A_done
	s_ff1_i32_b32 s0, s19
	s_bitset0_b32 s19, s0
	v_readlane_b32 s1, v20, s0
	s_lshl_b32 s1, s1, 11
	s_add_u32 s22, s14, s1
	s_addc_u32 s23, s15, 0
	global_load_dwordx2 v[72:73], v22, s[22:23]
	global_load_dwordx2 v[74:75], v22, s[22:23] offset:512
	global_load_dwordx2 v[76:77], v22, s[22:23] offset:1024
	global_load_dwordx2 v[78:79], v22, s[22:23] offset:1536
	s_bitset1_b32 s21, 2
.Lrp1_iss_A_done:
	s_cmp_eq_u32 s20, 0
	s_cbranch_scc1 .Lrp1_iss_B_done
	s_ff1_i32_b32 s0, s20
	s_bitset0_b32 s20, s0
	v_readlane_b32 s1, v21, s0
	s_lshl_b32 s1, s1, 11
	s_add_u32 s22, s14, s1
	s_addc_u32 s23, s15, 0
	global_load_dwordx2 v[80:81], v22, s[22:23]
	global_load_dwordx2 v[82:83], v22, s[22:23] offset:512
	global_load_dwordx2 v[84:85], v22, s[22:23] offset:1024
	global_load_dwordx2 v[86:87], v22, s[22:23] offset:1536
	s_bitset1_b32 s21, 3
	s_cmp_eq_u32 s20, 0
	s_cbranch_scc1 .Lrp1_iss_B_done
	s_ff1_i32_b32 s0, s20
	s_bitset0_b32 s20, s0
	v_readlane_b32 s1, v21, s0
	s_lshl_b32 s1, s1, 11
	s_add_u32 s22, s14, s1
	s_addc_u32 s23, s15, 0
	global_load_dwordx2 v[88:89], v22, s[22:23]
	global_load_dwordx2 v[90:91], v22, s[22:23] offset:512
	global_load_dwordx2 v[92:93], v22, s[22:23] offset:1024
	global_load_dwordx2 v[94:95], v22, s[22:23] offset:1536
	s_bitset1_b32 s21, 4
	s_cmp_eq_u32 s20, 0
	s_cbranch_scc1 .Lrp1_iss_B_done
	s_ff1_i32_b32 s0, s20
	s_bitset0_b32 s20, s0
	v_readlane_b32 s1, v21, s0
	s_lshl_b32 s1, s1, 11
	s_add_u32 s22, s14, s1
	s_addc_u32 s23, s15, 0
	global_load_dwordx2 v[96:97], v22, s[22:23]
	global_load_dwordx2 v[98:99], v22, s[22:23] offset:512
	global_load_dwordx2 v[100:101], v22, s[22:23] offset:1024
	global_load_dwordx2 v[102:103], v22, s[22:23] offset:1536
	s_bitset1_b32 s21, 5
.Lrp1_iss_B_done:
	s_waitcnt vmcnt(0)
	s_bitcmp1_b32 s21, 0
	s_cbranch_scc0 .Lrp1_add_skip_0
	v_lshlrev_b32_e32 v104, 16, v56
	v_and_b32_e32 v105, 0xffff0000, v56
	v_pk_add_f32 v[24:25], v[24:25], v[104:105]
	v_lshlrev_b32_e32 v106, 16, v57
	v_and_b32_e32 v107, 0xffff0000, v57
	v_pk_add_f32 v[26:27], v[26:27], v[106:107]
	v_lshlrev_b32_e32 v108, 16, v58
	v_and_b32_e32 v109, 0xffff0000, v58
	v_pk_add_f32 v[28:29], v[28:29], v[108:109]
	v_lshlrev_b32_e32 v110, 16, v59
	v_and_b32_e32 v111, 0xffff0000, v59
	v_pk_add_f32 v[30:31], v[30:31], v[110:111]
	v_lshlrev_b32_e32 v104, 16, v60
	v_and_b32_e32 v105, 0xffff0000, v60
	v_pk_add_f32 v[32:33], v[32:33], v[104:105]
	v_lshlrev_b32_e32 v106, 16, v61
	v_and_b32_e32 v107, 0xffff0000, v61
	v_pk_add_f32 v[34:35], v[34:35], v[106:107]
	v_lshlrev_b32_e32 v108, 16, v62
	v_and_b32_e32 v109, 0xffff0000, v62
	v_pk_add_f32 v[36:37], v[36:37], v[108:109]
	v_lshlrev_b32_e32 v110, 16, v63
	v_and_b32_e32 v111, 0xffff0000, v63
	v_pk_add_f32 v[38:39], v[38:39], v[110:111]
.Lrp1_add_skip_0:
	s_bitcmp1_b32 s21, 1
	s_cbranch_scc0 .Lrp1_add_skip_1
	v_lshlrev_b32_e32 v104, 16, v64
	v_and_b32_e32 v105, 0xffff0000, v64
	v_pk_add_f32 v[24:25], v[24:25], v[104:105]
	v_lshlrev_b32_e32 v106, 16, v65
	v_and_b32_e32 v107, 0xffff0000, v65
	v_pk_add_f32 v[26:27], v[26:27], v[106:107]
	v_lshlrev_b32_e32 v108, 16, v66
	v_and_b32_e32 v109, 0xffff0000, v66
	v_pk_add_f32 v[28:29], v[28:29], v[108:109]
	v_lshlrev_b32_e32 v110, 16, v67
	v_and_b32_e32 v111, 0xffff0000, v67
	v_pk_add_f32 v[30:31], v[30:31], v[110:111]
	v_lshlrev_b32_e32 v104, 16, v68
	v_and_b32_e32 v105, 0xffff0000, v68
	v_pk_add_f32 v[32:33], v[32:33], v[104:105]
	v_lshlrev_b32_e32 v106, 16, v69
	v_and_b32_e32 v107, 0xffff0000, v69
	v_pk_add_f32 v[34:35], v[34:35], v[106:107]
	v_lshlrev_b32_e32 v108, 16, v70
	v_and_b32_e32 v109, 0xffff0000, v70
	v_pk_add_f32 v[36:37], v[36:37], v[108:109]
	v_lshlrev_b32_e32 v110, 16, v71
	v_and_b32_e32 v111, 0xffff0000, v71
	v_pk_add_f32 v[38:39], v[38:39], v[110:111]
.Lrp1_add_skip_1:
	s_bitcmp1_b32 s21, 2
	s_cbranch_scc0 .Lrp1_add_skip_2
	v_lshlrev_b32_e32 v104, 16, v72
	v_and_b32_e32 v105, 0xffff0000, v72
	v_pk_add_f32 v[24:25], v[24:25], v[104:105]
	v_lshlrev_b32_e32 v106, 16, v73
	v_and_b32_e32 v107, 0xffff0000, v73
	v_pk_add_f32 v[26:27], v[26:27], v[106:107]
	v_lshlrev_b32_e32 v108, 16, v74
	v_and_b32_e32 v109, 0xffff0000, v74
	v_pk_add_f32 v[28:29], v[28:29], v[108:109]
	v_lshlrev_b32_e32 v110, 16, v75
	v_and_b32_e32 v111, 0xffff0000, v75
	v_pk_add_f32 v[30:31], v[30:31], v[110:111]
	v_lshlrev_b32_e32 v104, 16, v76
	v_and_b32_e32 v105, 0xffff0000, v76
	v_pk_add_f32 v[32:33], v[32:33], v[104:105]
	v_lshlrev_b32_e32 v106, 16, v77
	v_and_b32_e32 v107, 0xffff0000, v77
	v_pk_add_f32 v[34:35], v[34:35], v[106:107]
	v_lshlrev_b32_e32 v108, 16, v78
	v_and_b32_e32 v109, 0xffff0000, v78
	v_pk_add_f32 v[36:37], v[36:37], v[108:109]
	v_lshlrev_b32_e32 v110, 16, v79
	v_and_b32_e32 v111, 0xffff0000, v79
	v_pk_add_f32 v[38:39], v[38:39], v[110:111]
.Lrp1_add_skip_2:
	s_bitcmp1_b32 s21, 3
	s_cbranch_scc0 .Lrp1_add_skip_3
	v_lshlrev_b32_e32 v104, 16, v80
	v_and_b32_e32 v105, 0xffff0000, v80
	v_pk_add_f32 v[40:41], v[40:41], v[104:105]
	v_lshlrev_b32_e32 v106, 16, v81
	v_and_b32_e32 v107, 0xffff0000, v81
	v_pk_add_f32 v[42:43], v[42:43], v[106:107]
	v_lshlrev_b32_e32 v108, 16, v82
	v_and_b32_e32 v109, 0xffff0000, v82
	v_pk_add_f32 v[44:45], v[44:45], v[108:109]
	v_lshlrev_b32_e32 v110, 16, v83
	v_and_b32_e32 v111, 0xffff0000, v83
	v_pk_add_f32 v[46:47], v[46:47], v[110:111]
	v_lshlrev_b32_e32 v104, 16, v84
	v_and_b32_e32 v105, 0xffff0000, v84
	v_pk_add_f32 v[48:49], v[48:49], v[104:105]
	v_lshlrev_b32_e32 v106, 16, v85
	v_and_b32_e32 v107, 0xffff0000, v85
	v_pk_add_f32 v[50:51], v[50:51], v[106:107]
	v_lshlrev_b32_e32 v108, 16, v86
	v_and_b32_e32 v109, 0xffff0000, v86
	v_pk_add_f32 v[52:53], v[52:53], v[108:109]
	v_lshlrev_b32_e32 v110, 16, v87
	v_and_b32_e32 v111, 0xffff0000, v87
	v_pk_add_f32 v[54:55], v[54:55], v[110:111]
.Lrp1_add_skip_3:
	s_bitcmp1_b32 s21, 4
	s_cbranch_scc0 .Lrp1_add_skip_4
	v_lshlrev_b32_e32 v104, 16, v88
	v_and_b32_e32 v105, 0xffff0000, v88
	v_pk_add_f32 v[40:41], v[40:41], v[104:105]
	v_lshlrev_b32_e32 v106, 16, v89
	v_and_b32_e32 v107, 0xffff0000, v89
	v_pk_add_f32 v[42:43], v[42:43], v[106:107]
	v_lshlrev_b32_e32 v108, 16, v90
	v_and_b32_e32 v109, 0xffff0000, v90
	v_pk_add_f32 v[44:45], v[44:45], v[108:109]
	v_lshlrev_b32_e32 v110, 16, v91
	v_and_b32_e32 v111, 0xffff0000, v91
	v_pk_add_f32 v[46:47], v[46:47], v[110:111]
	v_lshlrev_b32_e32 v104, 16, v92
	v_and_b32_e32 v105, 0xffff0000, v92
	v_pk_add_f32 v[48:49], v[48:49], v[104:105]
	v_lshlrev_b32_e32 v106, 16, v93
	v_and_b32_e32 v107, 0xffff0000, v93
	v_pk_add_f32 v[50:51], v[50:51], v[106:107]
	v_lshlrev_b32_e32 v108, 16, v94
	v_and_b32_e32 v109, 0xffff0000, v94
	v_pk_add_f32 v[52:53], v[52:53], v[108:109]
	v_lshlrev_b32_e32 v110, 16, v95
	v_and_b32_e32 v111, 0xffff0000, v95
	v_pk_add_f32 v[54:55], v[54:55], v[110:111]
.Lrp1_add_skip_4:
	s_bitcmp1_b32 s21, 5
	s_cbranch_scc0 .Lrp1_add_skip_5
	v_lshlrev_b32_e32 v104, 16, v96
	v_and_b32_e32 v105, 0xffff0000, v96
	v_pk_add_f32 v[40:41], v[40:41], v[104:105]
	v_lshlrev_b32_e32 v106, 16, v97
	v_and_b32_e32 v107, 0xffff0000, v97
	v_pk_add_f32 v[42:43], v[42:43], v[106:107]
	v_lshlrev_b32_e32 v108, 16, v98
	v_and_b32_e32 v109, 0xffff0000, v98
	v_pk_add_f32 v[44:45], v[44:45], v[108:109]
	v_lshlrev_b32_e32 v110, 16, v99
	v_and_b32_e32 v111, 0xffff0000, v99
	v_pk_add_f32 v[46:47], v[46:47], v[110:111]
	v_lshlrev_b32_e32 v104, 16, v100
	v_and_b32_e32 v105, 0xffff0000, v100
	v_pk_add_f32 v[48:49], v[48:49], v[104:105]
	v_lshlrev_b32_e32 v106, 16, v101
	v_and_b32_e32 v107, 0xffff0000, v101
	v_pk_add_f32 v[50:51], v[50:51], v[106:107]
	v_lshlrev_b32_e32 v108, 16, v102
	v_and_b32_e32 v109, 0xffff0000, v102
	v_pk_add_f32 v[52:53], v[52:53], v[108:109]
	v_lshlrev_b32_e32 v110, 16, v103
	v_and_b32_e32 v111, 0xffff0000, v103
	v_pk_add_f32 v[54:55], v[54:55], v[110:111]
.Lrp1_add_skip_5:
	s_or_b32 s0, s19, s20
	s_cmp_lg_u32 s0, 0
	s_cbranch_scc1 .Lrp1_round
.Lrp1_rounds_done:
	v_mov_b32_e32 v65, 0x358637bd
	v_mov_b32_e32 v66, 0x260
	v_mul_f32_e32 v68, v25, v25
	v_mul_f32_e32 v69, v27, v27
	v_mul_f32_e32 v70, v29, v29
	v_mul_f32_e32 v71, v31, v31
	v_mul_f32_e32 v72, v33, v33
	v_mul_f32_e32 v73, v35, v35
	v_mul_f32_e32 v74, v37, v37
	v_mul_f32_e32 v75, v39, v39
	v_fmac_f32_e32 v68, v24, v24
	v_fmac_f32_e32 v69, v26, v26
	v_fmac_f32_e32 v70, v28, v28
	v_fmac_f32_e32 v71, v30, v30
	v_fmac_f32_e32 v72, v32, v32
	v_fmac_f32_e32 v73, v34, v34
	v_fmac_f32_e32 v74, v36, v36
	v_fmac_f32_e32 v75, v38, v38
	v_add_f32_e32 v68, v68, v69
	v_add_f32_e32 v70, v70, v71
	v_add_f32_e32 v72, v72, v73
	v_add_f32_e32 v74, v74, v75
	v_add_f32_e32 v56, v70, v68
	v_add_f32_e32 v56, v72, v56
	v_add_f32_e32 v56, v74, v56
	s_lshl_b32 s0, s2, 11
	s_add_u32 s22, s12, s0
	s_addc_u32 s23, s13, 0
	s_add_u32 s24, s6, s0
	s_addc_u32 s25, s7, 0
	v_cvt_pk_bf16_f32 v76, v24, v25
	v_cvt_pk_bf16_f32 v77, v26, v27
	global_store_dwordx2 v22, v[76:77], s[22:23]
	v_cvt_pk_bf16_f32 v78, v28, v29
	v_cvt_pk_bf16_f32 v79, v30, v31
	global_store_dwordx2 v22, v[78:79], s[22:23] offset:512
	v_cvt_pk_bf16_f32 v80, v32, v33
	v_cvt_pk_bf16_f32 v81, v34, v35
	global_store_dwordx2 v22, v[80:81], s[22:23] offset:1024
	v_cvt_pk_bf16_f32 v82, v36, v37
	v_cvt_pk_bf16_f32 v83, v38, v39
	global_store_dwordx2 v22, v[82:83], s[22:23] offset:1536
	s_nop 1
	v_add_f32_dpp v56, v56, v56 quad_perm:[1,0,3,2] row_mask:0xf bank_mask:0xf bound_ctrl:1
	s_nop 1
	v_add_f32_dpp v56, v56, v56 quad_perm:[2,3,0,1] row_mask:0xf bank_mask:0xf bound_ctrl:1
	s_nop 1
	v_add_f32_dpp v56, v56, v56 row_half_mirror row_mask:0xf bank_mask:0xf bound_ctrl:1
	s_nop 1
	v_add_f32_dpp v56, v56, v56 row_mirror row_mask:0xf bank_mask:0xf bound_ctrl:1
	v_mov_b32_e32 v57, v56
	s_nop 1
	v_permlane16_swap_b32_e32 v56, v57
	v_add_f32_e32 v56, v56, v57
	v_mov_b32_e32 v57, v56
	s_nop 1
	v_permlane32_swap_b32_e32 v56, v57
	v_add_f32_e32 v56, v56, v57
	v_fmamk_f32 v56, v56, 0x3a800000, v65
	v_mul_f32_e32 v57, 0x4f800000, v56
	s_mov_b32 s0, 0xf800000
	v_cmp_gt_f32_e32 vcc, s0, v56
	s_nop 1
	v_cndmask_b32_e32 v56, v56, v57, vcc
	v_sqrt_f32_e32 v57, v56
	s_nop 0
	v_add_u32_e32 v58, -1, v57
	v_add_u32_e32 v63, 1, v57
	v_fma_f32 v61, -v58, v57, v56
	v_fma_f32 v62, -v63, v57, v56
	v_cmp_ge_f32_e64 s[0:1], 0, v61
	s_nop 1
	v_cndmask_b32_e64 v57, v57, v58, s[0:1]
	v_cmp_lt_f32_e64 s[0:1], 0, v62
	s_nop 1
	v_cndmask_b32_e64 v57, v57, v63, s[0:1]
	v_mul_f32_e32 v58, 0x37800000, v57
	v_cndmask_b32_e32 v57, v57, v58, vcc
	v_cmp_class_f32_e32 vcc, v56, v66
	s_nop 1
	v_cndmask_b32_e32 v56, v57, v56, vcc
	v_div_scale_f32 v60, s[0:1], v56, v56, 1.0
	v_rcp_f32_e32 v61, v60
	v_div_scale_f32 v62, vcc, 1.0, v56, 1.0
	s_nop 0
	v_fma_f32 v63, -v60, v61, 1.0
	v_fmac_f32_e32 v61, v63, v61
	v_mul_f32_e32 v63, v62, v61
	v_fma_f32 v64, -v60, v63, v62
	v_fmac_f32_e32 v63, v64, v61
	v_fma_f32 v60, -v60, v63, v62
	v_div_fmas_f32 v60, v60, v61, v63
	v_div_fixup_f32 v60, v60, v56, 1.0
	v_pk_mul_f32 v[24:25], v[60:61], v[24:25] op_sel_hi:[0,1]
	v_pk_mul_f32 v[26:27], v[60:61], v[26:27] op_sel_hi:[0,1]
	v_pk_mul_f32 v[28:29], v[60:61], v[28:29] op_sel_hi:[0,1]
	v_pk_mul_f32 v[30:31], v[60:61], v[30:31] op_sel_hi:[0,1]
	v_pk_mul_f32 v[32:33], v[60:61], v[32:33] op_sel_hi:[0,1]
	v_pk_mul_f32 v[34:35], v[60:61], v[34:35] op_sel_hi:[0,1]
	v_pk_mul_f32 v[36:37], v[60:61], v[36:37] op_sel_hi:[0,1]
	v_pk_mul_f32 v[38:39], v[60:61], v[38:39] op_sel_hi:[0,1]
	v_cvt_pk_bf16_f32 v84, v24, v25
	v_cvt_pk_bf16_f32 v85, v26, v27
	global_store_dwordx2 v22, v[84:85], s[24:25]
	v_cvt_pk_bf16_f32 v86, v28, v29
	v_cvt_pk_bf16_f32 v87, v30, v31
	global_store_dwordx2 v22, v[86:87], s[24:25] offset:512
	v_cvt_pk_bf16_f32 v88, v32, v33
	v_cvt_pk_bf16_f32 v89, v34, v35
	global_store_dwordx2 v22, v[88:89], s[24:25] offset:1024
	v_cvt_pk_bf16_f32 v90, v36, v37
	v_cvt_pk_bf16_f32 v91, v38, v39
	global_store_dwordx2 v22, v[90:91], s[24:25] offset:1536
	s_cmp_eq_u32 s17, 0
	s_cbranch_scc1 .Lrp1_skipB
	v_mov_b32_e32 v65, 0x358637bd
	v_mov_b32_e32 v66, 0x260
	v_mul_f32_e32 v68, v41, v41
	v_mul_f32_e32 v69, v43, v43
	v_mul_f32_e32 v70, v45, v45
	v_mul_f32_e32 v71, v47, v47
	v_mul_f32_e32 v72, v49, v49
	v_mul_f32_e32 v73, v51, v51
	v_mul_f32_e32 v74, v53, v53
	v_mul_f32_e32 v75, v55, v55
	v_fmac_f32_e32 v68, v40, v40
	v_fmac_f32_e32 v69, v42, v42
	v_fmac_f32_e32 v70, v44, v44
	v_fmac_f32_e32 v71, v46, v46
	v_fmac_f32_e32 v72, v48, v48
	v_fmac_f32_e32 v73, v50, v50
	v_fmac_f32_e32 v74, v52, v52
	v_fmac_f32_e32 v75, v54, v54
	v_add_f32_e32 v68, v68, v69
	v_add_f32_e32 v70, v70, v71
	v_add_f32_e32 v72, v72, v73
	v_add_f32_e32 v74, v74, v75
	v_add_f32_e32 v56, v70, v68
	v_add_f32_e32 v56, v72, v56
	v_add_f32_e32 v56, v74, v56
	s_lshl_b32 s0, s3, 11
	s_add_u32 s22, s12, s0
	s_addc_u32 s23, s13, 0
	s_add_u32 s24, s6, s0
	s_addc_u32 s25, s7, 0
	v_cvt_pk_bf16_f32 v76, v40, v41
	v_cvt_pk_bf16_f32 v77, v42, v43
	global_store_dwordx2 v22, v[76:77], s[22:23]
	v_cvt_pk_bf16_f32 v78, v44, v45
	v_cvt_pk_bf16_f32 v79, v46, v47
	global_store_dwordx2 v22, v[78:79], s[22:23] offset:512
	v_cvt_pk_bf16_f32 v80, v48, v49
	v_cvt_pk_bf16_f32 v81, v50, v51
	global_store_dwordx2 v22, v[80:81], s[22:23] offset:1024
	v_cvt_pk_bf16_f32 v82, v52, v53
	v_cvt_pk_bf16_f32 v83, v54, v55
	global_store_dwordx2 v22, v[82:83], s[22:23] offset:1536
	s_nop 1
	v_add_f32_dpp v56, v56, v56 quad_perm:[1,0,3,2] row_mask:0xf bank_mask:0xf bound_ctrl:1
	s_nop 1
	v_add_f32_dpp v56, v56, v56 quad_perm:[2,3,0,1] row_mask:0xf bank_mask:0xf bound_ctrl:1
	s_nop 1
	v_add_f32_dpp v56, v56, v56 row_half_mirror row_mask:0xf bank_mask:0xf bound_ctrl:1
	s_nop 1
	v_add_f32_dpp v56, v56, v56 row_mirror row_mask:0xf bank_mask:0xf bound_ctrl:1
	v_mov_b32_e32 v57, v56
	s_nop 1
	v_permlane16_swap_b32_e32 v56, v57
	v_add_f32_e32 v56, v56, v57
	v_mov_b32_e32 v57, v56
	s_nop 1
	v_permlane32_swap_b32_e32 v56, v57
	v_add_f32_e32 v56, v56, v57
	v_fmamk_f32 v56, v56, 0x3a800000, v65
	v_mul_f32_e32 v57, 0x4f800000, v56
	s_mov_b32 s0, 0xf800000
	v_cmp_gt_f32_e32 vcc, s0, v56
	s_nop 1
	v_cndmask_b32_e32 v56, v56, v57, vcc
	v_sqrt_f32_e32 v57, v56
	s_nop 0
	v_add_u32_e32 v58, -1, v57
	v_add_u32_e32 v63, 1, v57
	v_fma_f32 v61, -v58, v57, v56
	v_fma_f32 v62, -v63, v57, v56
	v_cmp_ge_f32_e64 s[0:1], 0, v61
	s_nop 1
	v_cndmask_b32_e64 v57, v57, v58, s[0:1]
	v_cmp_lt_f32_e64 s[0:1], 0, v62
	s_nop 1
	v_cndmask_b32_e64 v57, v57, v63, s[0:1]
	v_mul_f32_e32 v58, 0x37800000, v57
	v_cndmask_b32_e32 v57, v57, v58, vcc
	v_cmp_class_f32_e32 vcc, v56, v66
	s_nop 1
	v_cndmask_b32_e32 v56, v57, v56, vcc
	v_div_scale_f32 v60, s[0:1], v56, v56, 1.0
	v_rcp_f32_e32 v61, v60
	v_div_scale_f32 v62, vcc, 1.0, v56, 1.0
	s_nop 0
	v_fma_f32 v63, -v60, v61, 1.0
	v_fmac_f32_e32 v61, v63, v61
	v_mul_f32_e32 v63, v62, v61
	v_fma_f32 v64, -v60, v63, v62
	v_fmac_f32_e32 v63, v64, v61
	v_fma_f32 v60, -v60, v63, v62
	v_div_fmas_f32 v60, v60, v61, v63
	v_div_fixup_f32 v60, v60, v56, 1.0
	v_pk_mul_f32 v[40:41], v[60:61], v[40:41] op_sel_hi:[0,1]
	v_pk_mul_f32 v[42:43], v[60:61], v[42:43] op_sel_hi:[0,1]
	v_pk_mul_f32 v[44:45], v[60:61], v[44:45] op_sel_hi:[0,1]
	v_pk_mul_f32 v[46:47], v[60:61], v[46:47] op_sel_hi:[0,1]
	v_pk_mul_f32 v[48:49], v[60:61], v[48:49] op_sel_hi:[0,1]
	v_pk_mul_f32 v[50:51], v[60:61], v[50:51] op_sel_hi:[0,1]
	v_pk_mul_f32 v[52:53], v[60:61], v[52:53] op_sel_hi:[0,1]
	v_pk_mul_f32 v[54:55], v[60:61], v[54:55] op_sel_hi:[0,1]
	v_cvt_pk_bf16_f32 v84, v40, v41
	v_cvt_pk_bf16_f32 v85, v42, v43
	global_store_dwordx2 v22, v[84:85], s[24:25]
	v_cvt_pk_bf16_f32 v86, v44, v45
	v_cvt_pk_bf16_f32 v87, v46, v47
	global_store_dwordx2 v22, v[86:87], s[24:25] offset:512
	v_cvt_pk_bf16_f32 v88, v48, v49
	v_cvt_pk_bf16_f32 v89, v50, v51
	global_store_dwordx2 v22, v[88:89], s[24:25] offset:1024
	v_cvt_pk_bf16_f32 v90, v52, v53
	v_cvt_pk_bf16_f32 v91, v54, v55
	global_store_dwordx2 v22, v[90:91], s[24:25] offset:1536
.Lrp1_skipB:
	s_add_i32 s2, s2, s16
	s_cmp_lt_i32 s2, 0x8000
	s_cbranch_scc1 .Lrp1_loop
